# MoE row-tile ready polls restricted to lane 0 of wave 0 (6 sites)
# speedup vs baseline: 1.0003x; 1.0003x over previous
.LBB0_1045:
	v_cmp_gt_u32_e64 s[4:5], 64, v0
	s_and_saveexec_b64 s[6:7], s[4:5]
	s_cbranch_execz .LBB0_1055
	s_mov_b64 exec, 1
	s_lshl_b32 s8, s68, 6
	s_ashr_i32 s9, s8, 31
	s_lshl_b64 s[8:9], s[8:9], 2
	v_readlane_b32 s1, v253, 42
	s_add_u32 s8, s1, s8
	v_readlane_b32 s1, v255, 7
	s_addc_u32 s9, s1, s9
	s_mov_b32 s1, 0x400001
	v_mov_b32_e32 v1, 0
	s_branch .LBB0_1048

.LBB0_1099:
	s_and_b64 s[0:1], s[10:11], exec
	s_cselect_b32 s65, s86, s21
	s_lshl_b32 s12, s68, 6
	s_ashr_i32 s13, s12, 31
	s_cmpk_lt_i32 s64, 0x81
	s_waitcnt vmcnt(0)
	v_lshl_add_u32 v130, s21, 2, v155
	s_mov_b64 s[14:15], -1
	s_cbranch_scc0 .LBB0_1113
	ds_read_b128 v[2:5], v201 offset:3072
	ds_read_b128 v[6:9], v201 offset:2048
	ds_read_b128 v[10:13], v201 offset:1024
	ds_read_b128 v[14:17], v201
	ds_read_b128 v[18:21], v202 offset:3072
	ds_read_b128 v[22:25], v202 offset:2048
	ds_read_b128 v[26:29], v202 offset:1024
	ds_read_b128 v[30:33], v202
	s_mov_b32 s67, s95
	ds_read_b128 v[34:37], v186
	ds_read_b128 v[38:41], v186 offset:1024
	ds_read_b128 v[42:45], v186 offset:2048
	ds_read_b128 v[46:49], v186 offset:3072
	ds_read_b128 v[50:53], v186 offset:4096
	ds_read_b128 v[54:57], v186 offset:5120
	ds_read2_b32 v[66:67], v130 offset0:2 offset1:3
	ds_read_b128 v[58:61], v186 offset:6144
	ds_read_b128 v[62:65], v186 offset:7168
	s_add_i32 s88, s71, 0xc000
	s_mov_b32 m0, s88
	s_add_i32 s89, s71, 0xe000
	s_waitcnt lgkmcnt(0)
	global_load_lds_dwordx4 v66, s[34:35]
	s_mov_b32 m0, s89
	s_nop 0
	global_load_lds_dwordx4 v67, s[34:35]
	s_waitcnt vmcnt(8)
	s_waitcnt lgkmcnt(0)
	s_barrier
	s_setprio 1
	v_mfma_f32_16x16x32_bf16 v[66:69], v[30:33], v[34:37], 0
	v_mfma_f32_16x16x32_bf16 v[72:75], v[26:29], v[38:41], v[66:69]
	v_mfma_f32_16x16x32_bf16 v[66:69], v[22:25], v[34:37], 0
	v_mfma_f32_16x16x32_bf16 v[76:79], v[18:21], v[38:41], v[66:69]
	v_mfma_f32_16x16x32_bf16 v[66:69], v[30:33], v[42:45], 0
	v_mfma_f32_16x16x32_bf16 v[80:83], v[26:29], v[46:49], v[66:69]
	v_mfma_f32_16x16x32_bf16 v[66:69], v[22:25], v[42:45], 0
	v_mfma_f32_16x16x32_bf16 v[84:87], v[18:21], v[46:49], v[66:69]
	v_mfma_f32_16x16x32_bf16 v[66:69], v[30:33], v[50:53], 0
	v_mfma_f32_16x16x32_bf16 v[88:91], v[26:29], v[54:57], v[66:69]
	v_mfma_f32_16x16x32_bf16 v[66:69], v[22:25], v[50:53], 0
	v_mfma_f32_16x16x32_bf16 v[30:33], v[30:33], v[58:61], 0
	v_mfma_f32_16x16x32_bf16 v[22:25], v[22:25], v[58:61], 0
	v_mfma_f32_16x16x32_bf16 v[92:95], v[18:21], v[54:57], v[66:69]
	v_mfma_f32_16x16x32_bf16 v[26:29], v[26:29], v[62:65], v[30:33]
	v_mfma_f32_16x16x32_bf16 v[18:21], v[18:21], v[62:65], v[22:25]
	s_setprio 0
	s_setprio 1
	v_mfma_f32_16x16x32_bf16 v[22:25], v[14:17], v[34:37], 0
	v_mfma_f32_16x16x32_bf16 v[30:33], v[6:9], v[34:37], 0
	v_mfma_f32_16x16x32_bf16 v[22:25], v[10:13], v[38:41], v[22:25]
	v_mfma_f32_16x16x32_bf16 v[30:33], v[2:5], v[38:41], v[30:33]
	v_mfma_f32_16x16x32_bf16 v[34:37], v[14:17], v[42:45], 0
	v_mfma_f32_16x16x32_bf16 v[38:41], v[6:9], v[42:45], 0
	v_mfma_f32_16x16x32_bf16 v[34:37], v[10:13], v[46:49], v[34:37]
	v_mfma_f32_16x16x32_bf16 v[38:41], v[2:5], v[46:49], v[38:41]
	v_mfma_f32_16x16x32_bf16 v[42:45], v[14:17], v[50:53], 0
	v_mfma_f32_16x16x32_bf16 v[46:49], v[6:9], v[50:53], 0
	v_mfma_f32_16x16x32_bf16 v[14:17], v[14:17], v[58:61], 0
	v_mfma_f32_16x16x32_bf16 v[6:9], v[6:9], v[58:61], 0
	v_mfma_f32_16x16x32_bf16 v[42:45], v[10:13], v[54:57], v[42:45]
	v_mfma_f32_16x16x32_bf16 v[46:49], v[2:5], v[54:57], v[46:49]
	v_mfma_f32_16x16x32_bf16 v[10:13], v[10:13], v[62:65], v[14:17]
	v_mfma_f32_16x16x32_bf16 v[2:5], v[2:5], v[62:65], v[6:9]
	s_setprio 0
	s_barrier
	s_add_i32 s90, s79, s70
	v_lshl_add_u64 v[66:67], s[8:9], 0, v[160:161]
	s_add_i32 s91, s90, 0x2000
	v_lshl_add_u64 v[6:7], v[66:67], 0, s[50:51]
	s_mov_b32 m0, s90
	v_lshl_add_u64 v[68:69], s[8:9], 0, v[162:163]
	s_add_u32 s0, s8, 0x200100
	global_load_lds_dwordx4 v[6:7], off
	v_lshl_add_u64 v[6:7], v[68:69], 0, s[50:51]
	s_mov_b32 m0, s91
	s_addc_u32 s1, s9, 0
	s_add_i32 s94, s78, s70
	global_load_lds_dwordx4 v[6:7], off
	v_lshl_add_u64 v[6:7], s[0:1], 0, v[160:161]
	s_mov_b32 m0, s94
	s_add_i32 s95, s94, 0x2000
	global_load_lds_dwordx4 v[6:7], off
	v_lshl_add_u64 v[6:7], s[0:1], 0, v[162:163]
	s_mov_b32 m0, s95
	s_nop 0
	global_load_lds_dwordx4 v[6:7], off
	ds_read2_b32 v[6:7], v130 offset1:1
	s_mov_b32 m0, s71
	s_waitcnt lgkmcnt(0)
	global_load_lds_dwordx4 v6, s[38:39]
	s_mov_b32 m0, s72
	s_nop 0
	global_load_lds_dwordx4 v7, s[38:39]
	s_waitcnt vmcnt(8)
	s_waitcnt lgkmcnt(0)
	s_barrier
	s_barrier
	s_add_i32 s97, 0, 0x18000
	s_add_i32 s0, 0, 0x1c000
	v_add_u32_e32 v70, s97, v159
	v_add_u32_e32 v71, s0, v159
	ds_read_b128 v[6:9], v70
	ds_read_b128 v[14:17], v70 offset:1024
	ds_read_b128 v[50:53], v70 offset:2048
	ds_read_b128 v[54:57], v70 offset:3072
	ds_read_b128 v[58:61], v71
	ds_read_b128 v[62:65], v71 offset:1024
	ds_read_b128 v[96:99], v71 offset:2048
	ds_read_b128 v[100:103], v71 offset:3072
	ds_read_b128 v[104:107], v186 offset:32768
	ds_read_b128 v[108:111], v186 offset:33792
	ds_read_b128 v[112:115], v186 offset:34816
	ds_read_b128 v[116:119], v186 offset:35840
	ds_read_b128 v[120:123], v186 offset:36864
	ds_read_b128 v[124:127], v186 offset:37888
	ds_read2_b32 v[128:129], v130 offset0:2 offset1:3
	ds_read_b128 v[132:135], v186 offset:38912
	ds_read_b128 v[136:139], v186 offset:39936
	s_mov_b32 m0, s73
	s_waitcnt lgkmcnt(0)
	global_load_lds_dwordx4 v128, s[38:39]
	s_mov_b32 m0, s74
	s_nop 0
	global_load_lds_dwordx4 v129, s[38:39]
	s_waitcnt vmcnt(8)
	s_waitcnt lgkmcnt(0)
	s_barrier
	s_setprio 1
	v_mfma_f32_16x16x32_bf16 v[72:75], v[6:9], v[104:107], v[72:75]
	v_mfma_f32_16x16x32_bf16 v[80:83], v[6:9], v[112:115], v[80:83]
	v_mfma_f32_16x16x32_bf16 v[88:91], v[6:9], v[120:123], v[88:91]
	v_mfma_f32_16x16x32_bf16 v[6:9], v[6:9], v[132:135], v[26:29]
	v_mfma_f32_16x16x32_bf16 v[72:75], v[14:17], v[108:111], v[72:75]
	v_mfma_f32_16x16x32_bf16 v[80:83], v[14:17], v[116:119], v[80:83]
	v_mfma_f32_16x16x32_bf16 v[88:91], v[14:17], v[124:127], v[88:91]
	v_mfma_f32_16x16x32_bf16 v[6:9], v[14:17], v[136:139], v[6:9]
	v_mfma_f32_16x16x32_bf16 v[14:17], v[50:53], v[132:135], v[18:21]
	v_mfma_f32_16x16x32_bf16 v[76:79], v[50:53], v[104:107], v[76:79]
	v_mfma_f32_16x16x32_bf16 v[84:87], v[50:53], v[112:115], v[84:87]
	v_mfma_f32_16x16x32_bf16 v[92:95], v[50:53], v[120:123], v[92:95]
	v_mfma_f32_16x16x32_bf16 v[14:17], v[54:57], v[136:139], v[14:17]
	v_mfma_f32_16x16x32_bf16 v[76:79], v[54:57], v[108:111], v[76:79]
	v_mfma_f32_16x16x32_bf16 v[84:87], v[54:57], v[116:119], v[84:87]
	v_mfma_f32_16x16x32_bf16 v[92:95], v[54:57], v[124:127], v[92:95]
	s_setprio 0
	s_setprio 1
	v_mfma_f32_16x16x32_bf16 v[18:21], v[58:61], v[104:107], v[22:25]
	v_mfma_f32_16x16x32_bf16 v[22:25], v[96:99], v[104:107], v[30:33]
	v_mfma_f32_16x16x32_bf16 v[26:29], v[58:61], v[112:115], v[34:37]
	v_mfma_f32_16x16x32_bf16 v[30:33], v[96:99], v[112:115], v[38:41]
	v_mfma_f32_16x16x32_bf16 v[34:37], v[58:61], v[120:123], v[42:45]
	v_mfma_f32_16x16x32_bf16 v[38:41], v[96:99], v[120:123], v[46:49]
	v_mfma_f32_16x16x32_bf16 v[10:13], v[58:61], v[132:135], v[10:13]
	v_mfma_f32_16x16x32_bf16 v[2:5], v[96:99], v[132:135], v[2:5]
	v_mfma_f32_16x16x32_bf16 v[18:21], v[62:65], v[108:111], v[18:21]
	v_mfma_f32_16x16x32_bf16 v[22:25], v[100:103], v[108:111], v[22:25]
	v_mfma_f32_16x16x32_bf16 v[26:29], v[62:65], v[116:119], v[26:29]
	v_mfma_f32_16x16x32_bf16 v[30:33], v[100:103], v[116:119], v[30:33]
	v_mfma_f32_16x16x32_bf16 v[34:37], v[62:65], v[124:127], v[34:37]
	v_mfma_f32_16x16x32_bf16 v[38:41], v[100:103], v[124:127], v[38:41]
	v_mfma_f32_16x16x32_bf16 v[10:13], v[62:65], v[136:139], v[10:13]
	v_mfma_f32_16x16x32_bf16 v[2:5], v[100:103], v[136:139], v[2:5]
	s_setprio 0
	s_barrier
	s_add_i32 s97, s97, s70
	s_add_i32 s96, s97, 0x2000
	v_lshl_add_u64 v[42:43], v[66:67], 0, s[52:53]
	s_mov_b32 m0, s97
	s_add_u32 s14, s8, 0x200180
	global_load_lds_dwordx4 v[42:43], off
	v_lshl_add_u64 v[42:43], v[68:69], 0, s[52:53]
	s_mov_b32 m0, s96
	s_addc_u32 s15, s9, 0
	s_add_i32 s0, s0, s70
	global_load_lds_dwordx4 v[42:43], off
	v_lshl_add_u64 v[42:43], s[14:15], 0, v[160:161]
	s_mov_b32 m0, s0
	s_add_i32 s1, s0, 0x2000
	global_load_lds_dwordx4 v[42:43], off
	v_lshl_add_u64 v[42:43], s[14:15], 0, v[162:163]
	s_mov_b32 m0, s1
	s_nop 0
	global_load_lds_dwordx4 v[42:43], off
	ds_read2_b32 v[42:43], v130 offset1:1
	s_mov_b32 m0, s75
	s_waitcnt lgkmcnt(0)
	global_load_lds_dwordx4 v42, s[40:41]
	s_mov_b32 m0, s76
	s_nop 0
	global_load_lds_dwordx4 v43, s[40:41]
	s_waitcnt vmcnt(8)
	s_waitcnt lgkmcnt(0)
	s_barrier
	s_barrier
	ds_read_b128 v[42:45], v201 offset:3072
	ds_read_b128 v[46:49], v201 offset:2048
	ds_read_b128 v[50:53], v201 offset:1024
	ds_read_b128 v[54:57], v201
	ds_read_b128 v[58:61], v202 offset:3072
	ds_read_b128 v[62:65], v202 offset:2048
	ds_read_b128 v[96:99], v202 offset:1024
	ds_read_b128 v[100:103], v202
	ds_read_b128 v[104:107], v186
	ds_read_b128 v[108:111], v186 offset:1024
	ds_read_b128 v[112:115], v186 offset:2048
	ds_read_b128 v[116:119], v186 offset:3072
	ds_read_b128 v[120:123], v186 offset:4096
	ds_read_b128 v[124:127], v186 offset:5120
	ds_read2_b32 v[128:129], v130 offset0:2 offset1:3
	ds_read_b128 v[132:135], v186 offset:6144
	ds_read_b128 v[136:139], v186 offset:7168
	s_mov_b32 m0, s88
	s_waitcnt lgkmcnt(0)
	global_load_lds_dwordx4 v128, s[40:41]
	s_mov_b32 m0, s89
	s_nop 0
	global_load_lds_dwordx4 v129, s[40:41]
	s_waitcnt vmcnt(8)
	s_waitcnt lgkmcnt(0)
	s_barrier
	s_setprio 1
	v_mfma_f32_16x16x32_bf16 v[6:9], v[100:103], v[132:135], v[6:9]
	v_mfma_f32_16x16x32_bf16 v[14:17], v[62:65], v[132:135], v[14:17]
	v_mfma_f32_16x16x32_bf16 v[72:75], v[100:103], v[104:107], v[72:75]
	v_mfma_f32_16x16x32_bf16 v[76:79], v[62:65], v[104:107], v[76:79]
	v_mfma_f32_16x16x32_bf16 v[80:83], v[100:103], v[112:115], v[80:83]
	v_mfma_f32_16x16x32_bf16 v[84:87], v[62:65], v[112:115], v[84:87]
	v_mfma_f32_16x16x32_bf16 v[88:91], v[100:103], v[120:123], v[88:91]
	v_mfma_f32_16x16x32_bf16 v[92:95], v[62:65], v[120:123], v[92:95]
	v_mfma_f32_16x16x32_bf16 v[6:9], v[96:99], v[136:139], v[6:9]
	v_mfma_f32_16x16x32_bf16 v[14:17], v[58:61], v[136:139], v[14:17]
	v_mfma_f32_16x16x32_bf16 v[72:75], v[96:99], v[108:111], v[72:75]
	v_mfma_f32_16x16x32_bf16 v[76:79], v[58:61], v[108:111], v[76:79]
	v_mfma_f32_16x16x32_bf16 v[80:83], v[96:99], v[116:119], v[80:83]
	v_mfma_f32_16x16x32_bf16 v[84:87], v[58:61], v[116:119], v[84:87]
	v_mfma_f32_16x16x32_bf16 v[88:91], v[96:99], v[124:127], v[88:91]
	v_mfma_f32_16x16x32_bf16 v[92:95], v[58:61], v[124:127], v[92:95]
	s_setprio 0
	s_setprio 1
	v_mfma_f32_16x16x32_bf16 v[18:21], v[54:57], v[104:107], v[18:21]
	v_mfma_f32_16x16x32_bf16 v[22:25], v[46:49], v[104:107], v[22:25]
	v_mfma_f32_16x16x32_bf16 v[26:29], v[54:57], v[112:115], v[26:29]
	v_mfma_f32_16x16x32_bf16 v[30:33], v[46:49], v[112:115], v[30:33]
	v_mfma_f32_16x16x32_bf16 v[34:37], v[54:57], v[120:123], v[34:37]
	v_mfma_f32_16x16x32_bf16 v[38:41], v[46:49], v[120:123], v[38:41]
	v_mfma_f32_16x16x32_bf16 v[10:13], v[54:57], v[132:135], v[10:13]
	v_mfma_f32_16x16x32_bf16 v[2:5], v[46:49], v[132:135], v[2:5]
	v_mfma_f32_16x16x32_bf16 v[18:21], v[50:53], v[108:111], v[18:21]
	v_mfma_f32_16x16x32_bf16 v[22:25], v[42:45], v[108:111], v[22:25]
	v_mfma_f32_16x16x32_bf16 v[26:29], v[50:53], v[116:119], v[26:29]
	v_mfma_f32_16x16x32_bf16 v[30:33], v[42:45], v[116:119], v[30:33]
	v_mfma_f32_16x16x32_bf16 v[34:37], v[50:53], v[124:127], v[34:37]
	v_mfma_f32_16x16x32_bf16 v[38:41], v[42:45], v[124:127], v[38:41]
	v_mfma_f32_16x16x32_bf16 v[10:13], v[50:53], v[136:139], v[10:13]
	v_mfma_f32_16x16x32_bf16 v[2:5], v[42:45], v[136:139], v[2:5]
	s_setprio 0
	s_barrier
	s_mov_b32 m0, s90
	v_lshl_add_u64 v[42:43], v[66:67], 0, s[54:55]
	s_add_u32 s14, s8, 0x200200
	global_load_lds_dwordx4 v[42:43], off
	v_lshl_add_u64 v[42:43], v[68:69], 0, s[54:55]
	s_mov_b32 m0, s91
	s_addc_u32 s15, s9, 0
	global_load_lds_dwordx4 v[42:43], off
	v_lshl_add_u64 v[42:43], s[14:15], 0, v[160:161]
	s_mov_b32 m0, s94
	s_nop 0
	global_load_lds_dwordx4 v[42:43], off
	v_lshl_add_u64 v[42:43], s[14:15], 0, v[162:163]
	s_mov_b32 m0, s95
	s_nop 0
	global_load_lds_dwordx4 v[42:43], off
	ds_read2_b32 v[42:43], v130 offset1:1
	s_mov_b32 m0, s71
	s_waitcnt lgkmcnt(0)
	global_load_lds_dwordx4 v42, s[42:43]
	s_mov_b32 m0, s72
	s_nop 0
	global_load_lds_dwordx4 v43, s[42:43]
	s_waitcnt vmcnt(8)
	s_waitcnt lgkmcnt(0)
	s_barrier
	s_barrier
	ds_read_b128 v[42:45], v70
	ds_read_b128 v[46:49], v70 offset:1024
	ds_read_b128 v[50:53], v70 offset:2048
	ds_read_b128 v[54:57], v70 offset:3072
	ds_read_b128 v[58:61], v71
	ds_read_b128 v[62:65], v71 offset:1024
	ds_read_b128 v[96:99], v71 offset:2048
	ds_read_b128 v[100:103], v71 offset:3072
	ds_read_b128 v[104:107], v186 offset:32768
	ds_read_b128 v[108:111], v186 offset:33792
	ds_read_b128 v[112:115], v186 offset:34816
	ds_read_b128 v[116:119], v186 offset:35840
	ds_read_b128 v[120:123], v186 offset:36864
	ds_read_b128 v[124:127], v186 offset:37888
	ds_read2_b32 v[128:129], v130 offset0:2 offset1:3
	ds_read_b128 v[132:135], v186 offset:38912
	ds_read_b128 v[136:139], v186 offset:39936
	s_mov_b32 m0, s73
	s_waitcnt lgkmcnt(0)
	global_load_lds_dwordx4 v128, s[42:43]
	s_mov_b32 m0, s74
	s_nop 0
	global_load_lds_dwordx4 v129, s[42:43]
	s_waitcnt vmcnt(8)
	s_waitcnt lgkmcnt(0)
	s_barrier
	s_setprio 1
	v_mfma_f32_16x16x32_bf16 v[6:9], v[42:45], v[132:135], v[6:9]
	v_mfma_f32_16x16x32_bf16 v[14:17], v[50:53], v[132:135], v[14:17]
	v_mfma_f32_16x16x32_bf16 v[72:75], v[42:45], v[104:107], v[72:75]
	v_mfma_f32_16x16x32_bf16 v[76:79], v[50:53], v[104:107], v[76:79]
	v_mfma_f32_16x16x32_bf16 v[80:83], v[42:45], v[112:115], v[80:83]
	v_mfma_f32_16x16x32_bf16 v[84:87], v[50:53], v[112:115], v[84:87]
	v_mfma_f32_16x16x32_bf16 v[88:91], v[42:45], v[120:123], v[88:91]
	v_mfma_f32_16x16x32_bf16 v[92:95], v[50:53], v[120:123], v[92:95]
	v_mfma_f32_16x16x32_bf16 v[6:9], v[46:49], v[136:139], v[6:9]
	v_mfma_f32_16x16x32_bf16 v[14:17], v[54:57], v[136:139], v[14:17]
	v_mfma_f32_16x16x32_bf16 v[72:75], v[46:49], v[108:111], v[72:75]
	v_mfma_f32_16x16x32_bf16 v[76:79], v[54:57], v[108:111], v[76:79]
	v_mfma_f32_16x16x32_bf16 v[80:83], v[46:49], v[116:119], v[80:83]
	v_mfma_f32_16x16x32_bf16 v[84:87], v[54:57], v[116:119], v[84:87]
	v_mfma_f32_16x16x32_bf16 v[88:91], v[46:49], v[124:127], v[88:91]
	v_mfma_f32_16x16x32_bf16 v[92:95], v[54:57], v[124:127], v[92:95]
	s_setprio 0
	s_setprio 1
	v_mfma_f32_16x16x32_bf16 v[18:21], v[58:61], v[104:107], v[18:21]
	v_mfma_f32_16x16x32_bf16 v[22:25], v[96:99], v[104:107], v[22:25]
	v_mfma_f32_16x16x32_bf16 v[26:29], v[58:61], v[112:115], v[26:29]
	v_mfma_f32_16x16x32_bf16 v[30:33], v[96:99], v[112:115], v[30:33]
	v_mfma_f32_16x16x32_bf16 v[34:37], v[58:61], v[120:123], v[34:37]
	v_mfma_f32_16x16x32_bf16 v[38:41], v[96:99], v[120:123], v[38:41]
	v_mfma_f32_16x16x32_bf16 v[10:13], v[58:61], v[132:135], v[10:13]
	v_mfma_f32_16x16x32_bf16 v[2:5], v[96:99], v[132:135], v[2:5]
	v_mfma_f32_16x16x32_bf16 v[18:21], v[62:65], v[108:111], v[18:21]
	v_mfma_f32_16x16x32_bf16 v[22:25], v[100:103], v[108:111], v[22:25]
	v_mfma_f32_16x16x32_bf16 v[26:29], v[62:65], v[116:119], v[26:29]
	v_mfma_f32_16x16x32_bf16 v[30:33], v[100:103], v[116:119], v[30:33]
	v_mfma_f32_16x16x32_bf16 v[34:37], v[62:65], v[124:127], v[34:37]
	v_mfma_f32_16x16x32_bf16 v[38:41], v[100:103], v[124:127], v[38:41]
	v_mfma_f32_16x16x32_bf16 v[10:13], v[62:65], v[136:139], v[10:13]
	v_mfma_f32_16x16x32_bf16 v[2:5], v[100:103], v[136:139], v[2:5]
	s_setprio 0
	s_barrier
	s_mov_b32 m0, s97
	v_lshl_add_u64 v[42:43], v[66:67], 0, s[56:57]
	s_add_u32 s14, s8, 0x200280
	global_load_lds_dwordx4 v[42:43], off
	v_lshl_add_u64 v[42:43], v[68:69], 0, s[56:57]
	s_mov_b32 m0, s96
	s_addc_u32 s15, s9, 0
	global_load_lds_dwordx4 v[42:43], off
	v_lshl_add_u64 v[42:43], s[14:15], 0, v[160:161]
	s_mov_b32 m0, s0
	s_nop 0
	global_load_lds_dwordx4 v[42:43], off
	v_lshl_add_u64 v[42:43], s[14:15], 0, v[162:163]
	s_mov_b32 m0, s1
	s_nop 0
	global_load_lds_dwordx4 v[42:43], off
	ds_read2_b32 v[42:43], v130 offset1:1
	s_mov_b32 m0, s75
	s_waitcnt lgkmcnt(0)
	global_load_lds_dwordx4 v42, s[44:45]
	s_mov_b32 m0, s76
	s_nop 0
	global_load_lds_dwordx4 v43, s[44:45]
	s_waitcnt vmcnt(8)
	s_waitcnt lgkmcnt(0)
	s_barrier
	s_barrier
	ds_read_b128 v[42:45], v201 offset:3072
	ds_read_b128 v[46:49], v201 offset:2048
	ds_read_b128 v[50:53], v201 offset:1024
	ds_read_b128 v[54:57], v201
	ds_read_b128 v[58:61], v202 offset:3072
	ds_read_b128 v[62:65], v202 offset:2048
	ds_read_b128 v[96:99], v202 offset:1024
	ds_read_b128 v[100:103], v202
	ds_read_b128 v[104:107], v186
	ds_read_b128 v[108:111], v186 offset:1024
	ds_read_b128 v[112:115], v186 offset:2048
	ds_read_b128 v[116:119], v186 offset:3072
	ds_read_b128 v[120:123], v186 offset:4096
	ds_read_b128 v[124:127], v186 offset:5120
	ds_read2_b32 v[128:129], v130 offset0:2 offset1:3
	ds_read_b128 v[132:135], v186 offset:6144
	ds_read_b128 v[136:139], v186 offset:7168
	s_mov_b32 m0, s88
	s_waitcnt lgkmcnt(0)
	global_load_lds_dwordx4 v128, s[44:45]
	s_mov_b32 m0, s89
	s_nop 0
	global_load_lds_dwordx4 v129, s[44:45]
	s_waitcnt vmcnt(8)
	s_waitcnt lgkmcnt(0)
	s_barrier
	s_setprio 1
	v_mfma_f32_16x16x32_bf16 v[72:75], v[100:103], v[104:107], v[72:75]
	v_mfma_f32_16x16x32_bf16 v[80:83], v[100:103], v[112:115], v[80:83]
	v_mfma_f32_16x16x32_bf16 v[88:91], v[100:103], v[120:123], v[88:91]
	v_mfma_f32_16x16x32_bf16 v[6:9], v[100:103], v[132:135], v[6:9]
	v_mfma_f32_16x16x32_bf16 v[72:75], v[96:99], v[108:111], v[72:75]
	v_mfma_f32_16x16x32_bf16 v[76:79], v[62:65], v[104:107], v[76:79]
	v_mfma_f32_16x16x32_bf16 v[80:83], v[96:99], v[116:119], v[80:83]
	v_mfma_f32_16x16x32_bf16 v[84:87], v[62:65], v[112:115], v[84:87]
	v_mfma_f32_16x16x32_bf16 v[88:91], v[96:99], v[124:127], v[88:91]
	v_mfma_f32_16x16x32_bf16 v[92:95], v[62:65], v[120:123], v[92:95]
	v_mfma_f32_16x16x32_bf16 v[96:99], v[96:99], v[136:139], v[6:9]
	v_mfma_f32_16x16x32_bf16 v[6:9], v[62:65], v[132:135], v[14:17]
	v_mfma_f32_16x16x32_bf16 v[76:79], v[58:61], v[108:111], v[76:79]
	v_mfma_f32_16x16x32_bf16 v[84:87], v[58:61], v[116:119], v[84:87]
	v_mfma_f32_16x16x32_bf16 v[92:95], v[58:61], v[124:127], v[92:95]
	v_mfma_f32_16x16x32_bf16 v[58:61], v[58:61], v[136:139], v[6:9]
	s_setprio 0
	s_setprio 1
	v_mfma_f32_16x16x32_bf16 v[6:9], v[54:57], v[104:107], v[18:21]
	v_mfma_f32_16x16x32_bf16 v[62:65], v[50:53], v[108:111], v[6:9]
	v_mfma_f32_16x16x32_bf16 v[6:9], v[46:49], v[104:107], v[22:25]
	v_mfma_f32_16x16x32_bf16 v[100:103], v[42:45], v[108:111], v[6:9]
	v_mfma_f32_16x16x32_bf16 v[6:9], v[54:57], v[112:115], v[26:29]
	v_mfma_f32_16x16x32_bf16 v[104:107], v[50:53], v[116:119], v[6:9]
	v_mfma_f32_16x16x32_bf16 v[6:9], v[46:49], v[112:115], v[30:33]
	v_mfma_f32_16x16x32_bf16 v[108:111], v[42:45], v[116:119], v[6:9]
	v_mfma_f32_16x16x32_bf16 v[6:9], v[54:57], v[120:123], v[34:37]
	v_mfma_f32_16x16x32_bf16 v[112:115], v[50:53], v[124:127], v[6:9]
	v_mfma_f32_16x16x32_bf16 v[6:9], v[46:49], v[120:123], v[38:41]
	v_mfma_f32_16x16x32_bf16 v[116:119], v[42:45], v[124:127], v[6:9]
	v_mfma_f32_16x16x32_bf16 v[6:9], v[54:57], v[132:135], v[10:13]
	v_mfma_f32_16x16x32_bf16 v[2:5], v[46:49], v[132:135], v[2:5]
	v_mfma_f32_16x16x32_bf16 v[120:123], v[50:53], v[136:139], v[6:9]
	v_mfma_f32_16x16x32_bf16 v[124:127], v[42:45], v[136:139], v[2:5]
	s_setprio 0
	s_barrier
	s_mov_b32 m0, s90
	s_nop 2
	v_lshl_add_u64 v[2:3], v[66:67], 0, s[58:59]
	s_add_u32 s14, s8, 0x200300
	global_load_lds_dwordx4 v[2:3], off
	v_lshl_add_u64 v[2:3], v[68:69], 0, s[58:59]
	s_mov_b32 m0, s91
	s_addc_u32 s15, s9, 0
	global_load_lds_dwordx4 v[2:3], off
	v_lshl_add_u64 v[2:3], s[14:15], 0, v[160:161]
	s_mov_b32 m0, s94
	s_nop 0
	global_load_lds_dwordx4 v[2:3], off
	v_lshl_add_u64 v[2:3], s[14:15], 0, v[162:163]
	s_mov_b32 m0, s95
	s_nop 0
	global_load_lds_dwordx4 v[2:3], off
	ds_read2_b32 v[2:3], v130 offset1:1
	s_mov_b32 m0, s71
	s_waitcnt lgkmcnt(0)
	global_load_lds_dwordx4 v2, s[46:47]
	s_mov_b32 m0, s72
	s_nop 0
	global_load_lds_dwordx4 v3, s[46:47]
	s_waitcnt vmcnt(8)
	s_waitcnt lgkmcnt(0)
	s_barrier
	s_barrier
	ds_read_b128 v[26:29], v70
	ds_read_b128 v[30:33], v70 offset:1024
	ds_read_b128 v[34:37], v70 offset:2048
	ds_read_b128 v[38:41], v70 offset:3072
	ds_read_b128 v[132:135], v71
	ds_read_b128 v[136:139], v71 offset:1024
	ds_read_b128 v[140:143], v71 offset:2048
	ds_read_b128 v[144:147], v71 offset:3072
	ds_read_b128 v[42:45], v186 offset:32768
	ds_read_b128 v[46:49], v186 offset:33792
	ds_read_b128 v[50:53], v186 offset:34816
	ds_read_b128 v[54:57], v186 offset:35840
	ds_read_b128 v[148:151], v186 offset:36864
	ds_read_b128 v[166:169], v186 offset:37888
	ds_read2_b32 v[2:3], v130 offset0:2 offset1:3
	ds_read_b128 v[170:173], v186 offset:38912
	ds_read_b128 v[174:177], v186 offset:39936
	s_mov_b32 m0, s73
	s_waitcnt lgkmcnt(0)
	global_load_lds_dwordx4 v2, s[46:47]
	s_mov_b32 m0, s74
	s_nop 0
	global_load_lds_dwordx4 v3, s[46:47]
	s_waitcnt vmcnt(8)
	s_waitcnt lgkmcnt(0)
	s_barrier
	s_setprio 1
	v_mfma_f32_16x16x32_bf16 v[2:5], v[26:29], v[42:45], v[72:75]
	v_mfma_f32_16x16x32_bf16 v[10:13], v[26:29], v[50:53], v[80:83]
	v_mfma_f32_16x16x32_bf16 v[18:21], v[26:29], v[148:151], v[88:91]
	v_mfma_f32_16x16x32_bf16 v[26:29], v[26:29], v[170:173], v[96:99]
	v_mfma_f32_16x16x32_bf16 v[2:5], v[30:33], v[46:49], v[2:5]
	v_mfma_f32_16x16x32_bf16 v[6:9], v[34:37], v[42:45], v[76:79]
	v_mfma_f32_16x16x32_bf16 v[10:13], v[30:33], v[54:57], v[10:13]
	v_mfma_f32_16x16x32_bf16 v[14:17], v[34:37], v[50:53], v[84:87]
	v_mfma_f32_16x16x32_bf16 v[18:21], v[30:33], v[166:169], v[18:21]
	v_mfma_f32_16x16x32_bf16 v[22:25], v[34:37], v[148:151], v[92:95]
	v_mfma_f32_16x16x32_bf16 v[26:29], v[30:33], v[174:177], v[26:29]
	v_mfma_f32_16x16x32_bf16 v[30:33], v[34:37], v[170:173], v[58:61]
	v_mfma_f32_16x16x32_bf16 v[6:9], v[38:41], v[46:49], v[6:9]
	v_mfma_f32_16x16x32_bf16 v[14:17], v[38:41], v[54:57], v[14:17]
	v_mfma_f32_16x16x32_bf16 v[22:25], v[38:41], v[166:169], v[22:25]
	v_mfma_f32_16x16x32_bf16 v[30:33], v[38:41], v[174:177], v[30:33]
	s_setprio 0
	s_setprio 1
	v_mfma_f32_16x16x32_bf16 v[34:37], v[132:135], v[42:45], v[62:65]
	v_mfma_f32_16x16x32_bf16 v[38:41], v[140:143], v[42:45], v[100:103]
	v_mfma_f32_16x16x32_bf16 v[34:37], v[136:139], v[46:49], v[34:37]
	v_mfma_f32_16x16x32_bf16 v[38:41], v[144:147], v[46:49], v[38:41]
	v_mfma_f32_16x16x32_bf16 v[42:45], v[132:135], v[50:53], v[104:107]
	v_mfma_f32_16x16x32_bf16 v[46:49], v[140:143], v[50:53], v[108:111]
	v_mfma_f32_16x16x32_bf16 v[42:45], v[136:139], v[54:57], v[42:45]
	v_mfma_f32_16x16x32_bf16 v[46:49], v[144:147], v[54:57], v[46:49]
	v_mfma_f32_16x16x32_bf16 v[50:53], v[132:135], v[148:151], v[112:115]
	v_mfma_f32_16x16x32_bf16 v[54:57], v[140:143], v[148:151], v[116:119]
	v_mfma_f32_16x16x32_bf16 v[58:61], v[132:135], v[170:173], v[120:123]
	v_mfma_f32_16x16x32_bf16 v[62:65], v[140:143], v[170:173], v[124:127]
	v_mfma_f32_16x16x32_bf16 v[50:53], v[136:139], v[166:169], v[50:53]
	v_mfma_f32_16x16x32_bf16 v[54:57], v[144:147], v[166:169], v[54:57]
	v_mfma_f32_16x16x32_bf16 v[58:61], v[136:139], v[174:177], v[58:61]
	v_mfma_f32_16x16x32_bf16 v[62:65], v[144:147], v[174:177], v[62:65]
	s_setprio 0
	s_barrier
	s_mov_b32 m0, s97
	v_lshl_add_u64 v[66:67], v[66:67], 0, s[60:61]
	s_add_u32 s14, s8, 0x200380
	global_load_lds_dwordx4 v[66:67], off
	v_lshl_add_u64 v[66:67], v[68:69], 0, s[60:61]
	s_mov_b32 m0, s96
	s_addc_u32 s15, s9, 0
	global_load_lds_dwordx4 v[66:67], off
	v_lshl_add_u64 v[66:67], s[14:15], 0, v[160:161]
	s_mov_b32 m0, s0
	s_nop 0
	global_load_lds_dwordx4 v[66:67], off
	v_lshl_add_u64 v[66:67], s[14:15], 0, v[162:163]
	s_mov_b32 m0, s1
	s_nop 0
	global_load_lds_dwordx4 v[66:67], off
	ds_read2_b32 v[66:67], v130 offset1:1
	s_mov_b32 m0, s75
	s_waitcnt lgkmcnt(0)
	global_load_lds_dwordx4 v66, s[48:49]
	s_mov_b32 m0, s76
	s_nop 0
	global_load_lds_dwordx4 v67, s[48:49]
	s_waitcnt vmcnt(8)
	s_waitcnt lgkmcnt(0)
	s_barrier
	s_barrier
	s_and_b64 vcc, exec, s[6:7]
	s_cbranch_vccnz .LBB0_1112
	s_and_saveexec_b64 s[14:15], s[4:5]
	s_cbranch_execz .LBB0_1111
	s_mov_b64 exec, 1
	s_lshl_b64 s[16:17], s[12:13], 2
	v_readlane_b32 s18, v253, 42
	s_add_u32 s16, s18, s16
	v_readlane_b32 s18, v255, 7
	s_addc_u32 s17, s18, s17
	s_mov_b32 s66, 0x400001
	s_branch .LBB0_1104

.LBB0_1115:
	s_cmp_eq_u32 s88, 6
	s_cselect_b64 s[14:15], -1, 0
	s_and_b64 s[0:1], s[10:11], s[14:15]
	s_andn2_b64 vcc, exec, s[0:1]
	s_cbranch_vccnz .LBB0_1127
	s_and_saveexec_b64 s[16:17], s[4:5]
	s_cbranch_execz .LBB0_1126
	s_mov_b64 exec, 1
	s_mov_b32 s0, 0x400001
	s_branch .LBB0_1119

.LBB0_2090:
	v_cmp_gt_u32_e64 s[0:1], 64, v0
	s_and_saveexec_b64 s[2:3], s[0:1]
	s_cbranch_execz .LBB0_2102
	s_mov_b64 exec, 1
	s_lshl_b32 s4, s62, 6
	s_ashr_i32 s5, s4, 31
	s_lshl_b64 s[4:5], s[4:5], 2
	s_add_u32 s4, s94, s4
	v_readlane_b32 s6, v253, 2
	s_addc_u32 s5, s6, s5
	s_mov_b32 s9, 0x400001
	v_mov_b32_e32 v0, 0
	s_branch .LBB0_2093

.LBB0_2146:
	s_and_b64 s[8:9], s[6:7], exec
	s_cselect_b32 s59, s81, s17
	s_lshl_b32 s8, s62, 6
	s_ashr_i32 s9, s8, 31
	s_cmpk_lt_i32 s58, 0x81
	s_waitcnt vmcnt(0)
	v_lshl_add_u32 v128, s17, 2, v155
	s_mov_b64 s[10:11], -1
	s_cbranch_scc0 .LBB0_2160
	ds_read_b128 v[0:3], v194 offset:3072
	ds_read_b128 v[4:7], v194 offset:2048
	ds_read_b128 v[8:11], v194 offset:1024
	ds_read_b128 v[12:15], v194
	ds_read_b128 v[16:19], v195 offset:3072
	ds_read_b128 v[20:23], v195 offset:2048
	ds_read_b128 v[24:27], v195 offset:1024
	ds_read_b128 v[28:31], v195
	ds_read_b128 v[32:35], v184
	ds_read_b128 v[36:39], v184 offset:1024
	ds_read_b128 v[40:43], v184 offset:2048
	ds_read_b128 v[44:47], v184 offset:3072
	ds_read_b128 v[48:51], v184 offset:4096
	ds_read_b128 v[52:55], v184 offset:5120
	ds_read2_b32 v[64:65], v128 offset0:2 offset1:3
	ds_read_b128 v[56:59], v184 offset:6144
	ds_read_b128 v[60:63], v184 offset:7168
	s_add_i32 s84, s67, 0xc000
	s_mov_b32 m0, s84
	s_add_i32 s85, s67, 0xe000
	s_waitcnt lgkmcnt(0)
	global_load_lds_dwordx4 v64, s[22:23]
	s_mov_b32 m0, s85
	s_nop 0
	global_load_lds_dwordx4 v65, s[22:23]
	s_waitcnt vmcnt(8)
	s_waitcnt lgkmcnt(0)
	s_barrier
	s_setprio 1
	v_mfma_f32_16x16x32_bf16 v[64:67], v[28:31], v[32:35], 0
	v_mfma_f32_16x16x32_bf16 v[70:73], v[24:27], v[36:39], v[64:67]
	v_mfma_f32_16x16x32_bf16 v[64:67], v[20:23], v[32:35], 0
	v_mfma_f32_16x16x32_bf16 v[74:77], v[16:19], v[36:39], v[64:67]
	v_mfma_f32_16x16x32_bf16 v[64:67], v[28:31], v[40:43], 0
	v_mfma_f32_16x16x32_bf16 v[78:81], v[24:27], v[44:47], v[64:67]
	v_mfma_f32_16x16x32_bf16 v[64:67], v[20:23], v[40:43], 0
	v_mfma_f32_16x16x32_bf16 v[82:85], v[16:19], v[44:47], v[64:67]
	v_mfma_f32_16x16x32_bf16 v[64:67], v[28:31], v[48:51], 0
	v_mfma_f32_16x16x32_bf16 v[86:89], v[24:27], v[52:55], v[64:67]
	v_mfma_f32_16x16x32_bf16 v[64:67], v[20:23], v[48:51], 0
	v_mfma_f32_16x16x32_bf16 v[28:31], v[28:31], v[56:59], 0
	v_mfma_f32_16x16x32_bf16 v[20:23], v[20:23], v[56:59], 0
	v_mfma_f32_16x16x32_bf16 v[90:93], v[16:19], v[52:55], v[64:67]
	v_mfma_f32_16x16x32_bf16 v[24:27], v[24:27], v[60:63], v[28:31]
	v_mfma_f32_16x16x32_bf16 v[16:19], v[16:19], v[60:63], v[20:23]
	s_setprio 0
	s_setprio 1
	v_mfma_f32_16x16x32_bf16 v[20:23], v[12:15], v[32:35], 0
	v_mfma_f32_16x16x32_bf16 v[28:31], v[4:7], v[32:35], 0
	v_mfma_f32_16x16x32_bf16 v[20:23], v[8:11], v[36:39], v[20:23]
	v_mfma_f32_16x16x32_bf16 v[28:31], v[0:3], v[36:39], v[28:31]
	v_mfma_f32_16x16x32_bf16 v[32:35], v[12:15], v[40:43], 0
	v_mfma_f32_16x16x32_bf16 v[36:39], v[4:7], v[40:43], 0
	v_mfma_f32_16x16x32_bf16 v[32:35], v[8:11], v[44:47], v[32:35]
	v_mfma_f32_16x16x32_bf16 v[36:39], v[0:3], v[44:47], v[36:39]
	v_mfma_f32_16x16x32_bf16 v[40:43], v[12:15], v[48:51], 0
	v_mfma_f32_16x16x32_bf16 v[44:47], v[4:7], v[48:51], 0
	v_mfma_f32_16x16x32_bf16 v[12:15], v[12:15], v[56:59], 0
	v_mfma_f32_16x16x32_bf16 v[4:7], v[4:7], v[56:59], 0
	v_mfma_f32_16x16x32_bf16 v[40:43], v[8:11], v[52:55], v[40:43]
	v_mfma_f32_16x16x32_bf16 v[44:47], v[0:3], v[52:55], v[44:47]
	v_mfma_f32_16x16x32_bf16 v[8:11], v[8:11], v[60:63], v[12:15]
	v_mfma_f32_16x16x32_bf16 v[0:3], v[0:3], v[60:63], v[4:7]
	s_setprio 0
	s_barrier
	v_lshl_add_u64 v[64:65], s[4:5], 0, v[156:157]
	s_mov_b64 s[10:11], 0x100
	s_add_i32 s86, s75, s66
	v_lshl_add_u64 v[4:5], v[64:65], 0, s[10:11]
	s_mov_b32 m0, s86
	v_lshl_add_u64 v[66:67], s[4:5], 0, v[158:159]
	s_add_i32 s87, s86, 0x2000
	global_load_lds_dwordx4 v[4:5], off
	v_lshl_add_u64 v[4:5], v[66:67], 0, s[10:11]
	s_add_u32 s10, s4, 0x200100
	s_mov_b32 m0, s87
	s_addc_u32 s11, s5, 0
	s_add_i32 s88, s74, s66
	global_load_lds_dwordx4 v[4:5], off
	v_lshl_add_u64 v[4:5], s[10:11], 0, v[156:157]
	s_mov_b32 m0, s88
	s_add_i32 s89, s88, 0x2000
	global_load_lds_dwordx4 v[4:5], off
	v_lshl_add_u64 v[4:5], s[10:11], 0, v[158:159]
	s_mov_b32 m0, s89
	s_nop 0
	global_load_lds_dwordx4 v[4:5], off
	ds_read2_b32 v[4:5], v128 offset1:1
	s_mov_b32 m0, s67
	s_waitcnt lgkmcnt(0)
	global_load_lds_dwordx4 v4, s[30:31]
	s_mov_b32 m0, s68
	s_nop 0
	global_load_lds_dwordx4 v5, s[30:31]
	s_waitcnt vmcnt(8)
	s_waitcnt lgkmcnt(0)
	s_barrier
	s_barrier
	s_add_i32 s91, 0, 0x18000
	s_add_i32 s92, 0, 0x1c000
	v_add_u32_e32 v68, s91, v181
	v_add_u32_e32 v69, s92, v181
	ds_read_b128 v[4:7], v68
	ds_read_b128 v[12:15], v68 offset:1024
	ds_read_b128 v[48:51], v68 offset:2048
	ds_read_b128 v[52:55], v68 offset:3072
	ds_read_b128 v[56:59], v69
	ds_read_b128 v[60:63], v69 offset:1024
	ds_read_b128 v[94:97], v69 offset:2048
	ds_read_b128 v[98:101], v69 offset:3072
	ds_read_b128 v[102:105], v184 offset:32768
	ds_read_b128 v[106:109], v184 offset:33792
	ds_read_b128 v[110:113], v184 offset:34816
	ds_read_b128 v[114:117], v184 offset:35840
	ds_read_b128 v[118:121], v184 offset:36864
	ds_read_b128 v[122:125], v184 offset:37888
	ds_read2_b32 v[126:127], v128 offset0:2 offset1:3
	ds_read_b128 v[130:133], v184 offset:38912
	ds_read_b128 v[134:137], v184 offset:39936
	s_mov_b32 m0, s69
	s_waitcnt lgkmcnt(0)
	global_load_lds_dwordx4 v126, s[30:31]
	s_mov_b32 m0, s70
	s_nop 0
	global_load_lds_dwordx4 v127, s[30:31]
	s_waitcnt vmcnt(8)
	s_waitcnt lgkmcnt(0)
	s_barrier
	s_setprio 1
	v_mfma_f32_16x16x32_bf16 v[70:73], v[4:7], v[102:105], v[70:73]
	v_mfma_f32_16x16x32_bf16 v[78:81], v[4:7], v[110:113], v[78:81]
	v_mfma_f32_16x16x32_bf16 v[86:89], v[4:7], v[118:121], v[86:89]
	v_mfma_f32_16x16x32_bf16 v[4:7], v[4:7], v[130:133], v[24:27]
	v_mfma_f32_16x16x32_bf16 v[70:73], v[12:15], v[106:109], v[70:73]
	v_mfma_f32_16x16x32_bf16 v[78:81], v[12:15], v[114:117], v[78:81]
	v_mfma_f32_16x16x32_bf16 v[86:89], v[12:15], v[122:125], v[86:89]
	v_mfma_f32_16x16x32_bf16 v[4:7], v[12:15], v[134:137], v[4:7]
	v_mfma_f32_16x16x32_bf16 v[12:15], v[48:51], v[130:133], v[16:19]
	v_mfma_f32_16x16x32_bf16 v[74:77], v[48:51], v[102:105], v[74:77]
	v_mfma_f32_16x16x32_bf16 v[82:85], v[48:51], v[110:113], v[82:85]
	v_mfma_f32_16x16x32_bf16 v[90:93], v[48:51], v[118:121], v[90:93]
	v_mfma_f32_16x16x32_bf16 v[12:15], v[52:55], v[134:137], v[12:15]
	v_mfma_f32_16x16x32_bf16 v[74:77], v[52:55], v[106:109], v[74:77]
	v_mfma_f32_16x16x32_bf16 v[82:85], v[52:55], v[114:117], v[82:85]
	v_mfma_f32_16x16x32_bf16 v[90:93], v[52:55], v[122:125], v[90:93]
	s_setprio 0
	s_setprio 1
	v_mfma_f32_16x16x32_bf16 v[16:19], v[56:59], v[102:105], v[20:23]
	v_mfma_f32_16x16x32_bf16 v[20:23], v[94:97], v[102:105], v[28:31]
	v_mfma_f32_16x16x32_bf16 v[24:27], v[56:59], v[110:113], v[32:35]
	v_mfma_f32_16x16x32_bf16 v[28:31], v[94:97], v[110:113], v[36:39]
	v_mfma_f32_16x16x32_bf16 v[32:35], v[56:59], v[118:121], v[40:43]
	v_mfma_f32_16x16x32_bf16 v[36:39], v[94:97], v[118:121], v[44:47]
	v_mfma_f32_16x16x32_bf16 v[8:11], v[56:59], v[130:133], v[8:11]
	v_mfma_f32_16x16x32_bf16 v[0:3], v[94:97], v[130:133], v[0:3]
	v_mfma_f32_16x16x32_bf16 v[16:19], v[60:63], v[106:109], v[16:19]
	v_mfma_f32_16x16x32_bf16 v[20:23], v[98:101], v[106:109], v[20:23]
	v_mfma_f32_16x16x32_bf16 v[24:27], v[60:63], v[114:117], v[24:27]
	v_mfma_f32_16x16x32_bf16 v[28:31], v[98:101], v[114:117], v[28:31]
	v_mfma_f32_16x16x32_bf16 v[32:35], v[60:63], v[122:125], v[32:35]
	v_mfma_f32_16x16x32_bf16 v[36:39], v[98:101], v[122:125], v[36:39]
	v_mfma_f32_16x16x32_bf16 v[8:11], v[60:63], v[134:137], v[8:11]
	v_mfma_f32_16x16x32_bf16 v[0:3], v[98:101], v[134:137], v[0:3]
	s_setprio 0
	s_barrier
	s_mov_b64 s[10:11], 0x180
	s_add_i32 s91, s91, s66
	v_lshl_add_u64 v[40:41], v[64:65], 0, s[10:11]
	s_mov_b32 m0, s91
	s_add_i32 s90, s91, 0x2000
	global_load_lds_dwordx4 v[40:41], off
	v_lshl_add_u64 v[40:41], v[66:67], 0, s[10:11]
	s_add_u32 s10, s4, 0x200180
	s_mov_b32 m0, s90
	s_addc_u32 s11, s5, 0
	s_add_i32 s92, s92, s66
	global_load_lds_dwordx4 v[40:41], off
	v_lshl_add_u64 v[40:41], s[10:11], 0, v[156:157]
	s_mov_b32 m0, s92
	s_add_i32 s93, s92, 0x2000
	global_load_lds_dwordx4 v[40:41], off
	v_lshl_add_u64 v[40:41], s[10:11], 0, v[158:159]
	s_mov_b32 m0, s93
	s_nop 0
	global_load_lds_dwordx4 v[40:41], off
	ds_read2_b32 v[40:41], v128 offset1:1
	s_mov_b32 m0, s71
	s_waitcnt lgkmcnt(0)
	global_load_lds_dwordx4 v40, s[34:35]
	s_mov_b32 m0, s72
	s_nop 0
	global_load_lds_dwordx4 v41, s[34:35]
	s_waitcnt vmcnt(8)
	s_waitcnt lgkmcnt(0)
	s_barrier
	s_barrier
	ds_read_b128 v[40:43], v194 offset:3072
	ds_read_b128 v[44:47], v194 offset:2048
	ds_read_b128 v[48:51], v194 offset:1024
	ds_read_b128 v[52:55], v194
	ds_read_b128 v[56:59], v195 offset:3072
	ds_read_b128 v[60:63], v195 offset:2048
	ds_read_b128 v[94:97], v195 offset:1024
	ds_read_b128 v[98:101], v195
	ds_read_b128 v[102:105], v184
	ds_read_b128 v[106:109], v184 offset:1024
	ds_read_b128 v[110:113], v184 offset:2048
	ds_read_b128 v[114:117], v184 offset:3072
	ds_read_b128 v[118:121], v184 offset:4096
	ds_read_b128 v[122:125], v184 offset:5120
	ds_read2_b32 v[126:127], v128 offset0:2 offset1:3
	ds_read_b128 v[130:133], v184 offset:6144
	ds_read_b128 v[134:137], v184 offset:7168
	s_mov_b32 m0, s84
	s_waitcnt lgkmcnt(0)
	global_load_lds_dwordx4 v126, s[34:35]
	s_mov_b32 m0, s85
	s_nop 0
	global_load_lds_dwordx4 v127, s[34:35]
	s_waitcnt vmcnt(8)
	s_waitcnt lgkmcnt(0)
	s_barrier
	s_setprio 1
	v_mfma_f32_16x16x32_bf16 v[4:7], v[98:101], v[130:133], v[4:7]
	v_mfma_f32_16x16x32_bf16 v[12:15], v[60:63], v[130:133], v[12:15]
	v_mfma_f32_16x16x32_bf16 v[70:73], v[98:101], v[102:105], v[70:73]
	v_mfma_f32_16x16x32_bf16 v[74:77], v[60:63], v[102:105], v[74:77]
	v_mfma_f32_16x16x32_bf16 v[78:81], v[98:101], v[110:113], v[78:81]
	v_mfma_f32_16x16x32_bf16 v[82:85], v[60:63], v[110:113], v[82:85]
	v_mfma_f32_16x16x32_bf16 v[86:89], v[98:101], v[118:121], v[86:89]
	v_mfma_f32_16x16x32_bf16 v[90:93], v[60:63], v[118:121], v[90:93]
	v_mfma_f32_16x16x32_bf16 v[4:7], v[94:97], v[134:137], v[4:7]
	v_mfma_f32_16x16x32_bf16 v[12:15], v[56:59], v[134:137], v[12:15]
	v_mfma_f32_16x16x32_bf16 v[70:73], v[94:97], v[106:109], v[70:73]
	v_mfma_f32_16x16x32_bf16 v[74:77], v[56:59], v[106:109], v[74:77]
	v_mfma_f32_16x16x32_bf16 v[78:81], v[94:97], v[114:117], v[78:81]
	v_mfma_f32_16x16x32_bf16 v[82:85], v[56:59], v[114:117], v[82:85]
	v_mfma_f32_16x16x32_bf16 v[86:89], v[94:97], v[122:125], v[86:89]
	v_mfma_f32_16x16x32_bf16 v[90:93], v[56:59], v[122:125], v[90:93]
	s_setprio 0
	s_setprio 1
	v_mfma_f32_16x16x32_bf16 v[16:19], v[52:55], v[102:105], v[16:19]
	v_mfma_f32_16x16x32_bf16 v[20:23], v[44:47], v[102:105], v[20:23]
	v_mfma_f32_16x16x32_bf16 v[24:27], v[52:55], v[110:113], v[24:27]
	v_mfma_f32_16x16x32_bf16 v[28:31], v[44:47], v[110:113], v[28:31]
	v_mfma_f32_16x16x32_bf16 v[32:35], v[52:55], v[118:121], v[32:35]
	v_mfma_f32_16x16x32_bf16 v[36:39], v[44:47], v[118:121], v[36:39]
	v_mfma_f32_16x16x32_bf16 v[8:11], v[52:55], v[130:133], v[8:11]
	v_mfma_f32_16x16x32_bf16 v[0:3], v[44:47], v[130:133], v[0:3]
	v_mfma_f32_16x16x32_bf16 v[16:19], v[48:51], v[106:109], v[16:19]
	v_mfma_f32_16x16x32_bf16 v[20:23], v[40:43], v[106:109], v[20:23]
	v_mfma_f32_16x16x32_bf16 v[24:27], v[48:51], v[114:117], v[24:27]
	v_mfma_f32_16x16x32_bf16 v[28:31], v[40:43], v[114:117], v[28:31]
	v_mfma_f32_16x16x32_bf16 v[32:35], v[48:51], v[122:125], v[32:35]
	v_mfma_f32_16x16x32_bf16 v[36:39], v[40:43], v[122:125], v[36:39]
	v_mfma_f32_16x16x32_bf16 v[8:11], v[48:51], v[134:137], v[8:11]
	v_mfma_f32_16x16x32_bf16 v[0:3], v[40:43], v[134:137], v[0:3]
	s_setprio 0
	s_barrier
	s_mov_b64 s[10:11], 0x200
	s_mov_b32 m0, s86
	v_lshl_add_u64 v[40:41], v[64:65], 0, s[10:11]
	global_load_lds_dwordx4 v[40:41], off
	v_lshl_add_u64 v[40:41], v[66:67], 0, s[10:11]
	s_add_u32 s10, s4, 0x200200
	s_mov_b32 m0, s87
	s_addc_u32 s11, s5, 0
	global_load_lds_dwordx4 v[40:41], off
	v_lshl_add_u64 v[40:41], s[10:11], 0, v[156:157]
	s_mov_b32 m0, s88
	s_nop 0
	global_load_lds_dwordx4 v[40:41], off
	v_lshl_add_u64 v[40:41], s[10:11], 0, v[158:159]
	s_mov_b32 m0, s89
	s_nop 0
	global_load_lds_dwordx4 v[40:41], off
	ds_read2_b32 v[40:41], v128 offset1:1
	s_mov_b32 m0, s67
	s_waitcnt lgkmcnt(0)
	global_load_lds_dwordx4 v40, s[96:97]
	s_mov_b32 m0, s68
	s_nop 0
	global_load_lds_dwordx4 v41, s[96:97]
	s_waitcnt vmcnt(8)
	s_waitcnt lgkmcnt(0)
	s_barrier
	s_barrier
	ds_read_b128 v[40:43], v68
	ds_read_b128 v[44:47], v68 offset:1024
	ds_read_b128 v[48:51], v68 offset:2048
	ds_read_b128 v[52:55], v68 offset:3072
	ds_read_b128 v[56:59], v69
	ds_read_b128 v[60:63], v69 offset:1024
	ds_read_b128 v[94:97], v69 offset:2048
	ds_read_b128 v[98:101], v69 offset:3072
	ds_read_b128 v[102:105], v184 offset:32768
	ds_read_b128 v[106:109], v184 offset:33792
	ds_read_b128 v[110:113], v184 offset:34816
	ds_read_b128 v[114:117], v184 offset:35840
	ds_read_b128 v[118:121], v184 offset:36864
	ds_read_b128 v[122:125], v184 offset:37888
	ds_read2_b32 v[126:127], v128 offset0:2 offset1:3
	ds_read_b128 v[130:133], v184 offset:38912
	ds_read_b128 v[134:137], v184 offset:39936
	s_mov_b32 m0, s69
	s_waitcnt lgkmcnt(0)
	global_load_lds_dwordx4 v126, s[96:97]
	s_mov_b32 m0, s70
	s_nop 0
	global_load_lds_dwordx4 v127, s[96:97]
	s_waitcnt vmcnt(8)
	s_waitcnt lgkmcnt(0)
	s_barrier
	s_setprio 1
	v_mfma_f32_16x16x32_bf16 v[4:7], v[40:43], v[130:133], v[4:7]
	v_mfma_f32_16x16x32_bf16 v[12:15], v[48:51], v[130:133], v[12:15]
	v_mfma_f32_16x16x32_bf16 v[70:73], v[40:43], v[102:105], v[70:73]
	v_mfma_f32_16x16x32_bf16 v[74:77], v[48:51], v[102:105], v[74:77]
	v_mfma_f32_16x16x32_bf16 v[78:81], v[40:43], v[110:113], v[78:81]
	v_mfma_f32_16x16x32_bf16 v[82:85], v[48:51], v[110:113], v[82:85]
	v_mfma_f32_16x16x32_bf16 v[86:89], v[40:43], v[118:121], v[86:89]
	v_mfma_f32_16x16x32_bf16 v[90:93], v[48:51], v[118:121], v[90:93]
	v_mfma_f32_16x16x32_bf16 v[4:7], v[44:47], v[134:137], v[4:7]
	v_mfma_f32_16x16x32_bf16 v[12:15], v[52:55], v[134:137], v[12:15]
	v_mfma_f32_16x16x32_bf16 v[70:73], v[44:47], v[106:109], v[70:73]
	v_mfma_f32_16x16x32_bf16 v[74:77], v[52:55], v[106:109], v[74:77]
	v_mfma_f32_16x16x32_bf16 v[78:81], v[44:47], v[114:117], v[78:81]
	v_mfma_f32_16x16x32_bf16 v[82:85], v[52:55], v[114:117], v[82:85]
	v_mfma_f32_16x16x32_bf16 v[86:89], v[44:47], v[122:125], v[86:89]
	v_mfma_f32_16x16x32_bf16 v[90:93], v[52:55], v[122:125], v[90:93]
	s_setprio 0
	s_setprio 1
	v_mfma_f32_16x16x32_bf16 v[16:19], v[56:59], v[102:105], v[16:19]
	v_mfma_f32_16x16x32_bf16 v[20:23], v[94:97], v[102:105], v[20:23]
	v_mfma_f32_16x16x32_bf16 v[24:27], v[56:59], v[110:113], v[24:27]
	v_mfma_f32_16x16x32_bf16 v[28:31], v[94:97], v[110:113], v[28:31]
	v_mfma_f32_16x16x32_bf16 v[32:35], v[56:59], v[118:121], v[32:35]
	v_mfma_f32_16x16x32_bf16 v[36:39], v[94:97], v[118:121], v[36:39]
	v_mfma_f32_16x16x32_bf16 v[8:11], v[56:59], v[130:133], v[8:11]
	v_mfma_f32_16x16x32_bf16 v[0:3], v[94:97], v[130:133], v[0:3]
	v_mfma_f32_16x16x32_bf16 v[16:19], v[60:63], v[106:109], v[16:19]
	v_mfma_f32_16x16x32_bf16 v[20:23], v[98:101], v[106:109], v[20:23]
	v_mfma_f32_16x16x32_bf16 v[24:27], v[60:63], v[114:117], v[24:27]
	v_mfma_f32_16x16x32_bf16 v[28:31], v[98:101], v[114:117], v[28:31]
	v_mfma_f32_16x16x32_bf16 v[32:35], v[60:63], v[122:125], v[32:35]
	v_mfma_f32_16x16x32_bf16 v[36:39], v[98:101], v[122:125], v[36:39]
	v_mfma_f32_16x16x32_bf16 v[8:11], v[60:63], v[134:137], v[8:11]
	v_mfma_f32_16x16x32_bf16 v[0:3], v[98:101], v[134:137], v[0:3]
	s_setprio 0
	s_barrier
	s_mov_b64 s[10:11], 0x280
	s_mov_b32 m0, s91
	v_lshl_add_u64 v[40:41], v[64:65], 0, s[10:11]
	global_load_lds_dwordx4 v[40:41], off
	v_lshl_add_u64 v[40:41], v[66:67], 0, s[10:11]
	s_add_u32 s10, s4, 0x200280
	s_mov_b32 m0, s90
	s_addc_u32 s11, s5, 0
	global_load_lds_dwordx4 v[40:41], off
	v_lshl_add_u64 v[40:41], s[10:11], 0, v[156:157]
	s_mov_b32 m0, s92
	s_nop 0
	global_load_lds_dwordx4 v[40:41], off
	v_lshl_add_u64 v[40:41], s[10:11], 0, v[158:159]
	s_mov_b32 m0, s93
	s_nop 0
	global_load_lds_dwordx4 v[40:41], off
	ds_read2_b32 v[40:41], v128 offset1:1
	s_mov_b32 m0, s71
	s_waitcnt lgkmcnt(0)
	global_load_lds_dwordx4 v40, s[60:61]
	s_mov_b32 m0, s72
	s_nop 0
	global_load_lds_dwordx4 v41, s[60:61]
	s_waitcnt vmcnt(8)
	s_waitcnt lgkmcnt(0)
	s_barrier
	s_barrier
	ds_read_b128 v[40:43], v194 offset:3072
	ds_read_b128 v[44:47], v194 offset:2048
	ds_read_b128 v[48:51], v194 offset:1024
	ds_read_b128 v[52:55], v194
	ds_read_b128 v[56:59], v195 offset:3072
	ds_read_b128 v[60:63], v195 offset:2048
	ds_read_b128 v[94:97], v195 offset:1024
	ds_read_b128 v[98:101], v195
	ds_read_b128 v[102:105], v184
	ds_read_b128 v[106:109], v184 offset:1024
	ds_read_b128 v[110:113], v184 offset:2048
	ds_read_b128 v[114:117], v184 offset:3072
	ds_read_b128 v[118:121], v184 offset:4096
	ds_read_b128 v[122:125], v184 offset:5120
	ds_read2_b32 v[126:127], v128 offset0:2 offset1:3
	ds_read_b128 v[130:133], v184 offset:6144
	ds_read_b128 v[134:137], v184 offset:7168
	s_mov_b32 m0, s84
	s_waitcnt lgkmcnt(0)
	global_load_lds_dwordx4 v126, s[60:61]
	s_mov_b32 m0, s85
	s_nop 0
	global_load_lds_dwordx4 v127, s[60:61]
	s_waitcnt vmcnt(8)
	s_waitcnt lgkmcnt(0)
	s_barrier
	s_setprio 1
	v_mfma_f32_16x16x32_bf16 v[70:73], v[98:101], v[102:105], v[70:73]
	v_mfma_f32_16x16x32_bf16 v[78:81], v[98:101], v[110:113], v[78:81]
	v_mfma_f32_16x16x32_bf16 v[86:89], v[98:101], v[118:121], v[86:89]
	v_mfma_f32_16x16x32_bf16 v[4:7], v[98:101], v[130:133], v[4:7]
	v_mfma_f32_16x16x32_bf16 v[70:73], v[94:97], v[106:109], v[70:73]
	v_mfma_f32_16x16x32_bf16 v[74:77], v[60:63], v[102:105], v[74:77]
	v_mfma_f32_16x16x32_bf16 v[78:81], v[94:97], v[114:117], v[78:81]
	v_mfma_f32_16x16x32_bf16 v[82:85], v[60:63], v[110:113], v[82:85]
	v_mfma_f32_16x16x32_bf16 v[86:89], v[94:97], v[122:125], v[86:89]
	v_mfma_f32_16x16x32_bf16 v[90:93], v[60:63], v[118:121], v[90:93]
	v_mfma_f32_16x16x32_bf16 v[94:97], v[94:97], v[134:137], v[4:7]
	v_mfma_f32_16x16x32_bf16 v[4:7], v[60:63], v[130:133], v[12:15]
	v_mfma_f32_16x16x32_bf16 v[74:77], v[56:59], v[106:109], v[74:77]
	v_mfma_f32_16x16x32_bf16 v[82:85], v[56:59], v[114:117], v[82:85]
	v_mfma_f32_16x16x32_bf16 v[90:93], v[56:59], v[122:125], v[90:93]
	v_mfma_f32_16x16x32_bf16 v[56:59], v[56:59], v[134:137], v[4:7]
	s_setprio 0
	s_setprio 1
	v_mfma_f32_16x16x32_bf16 v[4:7], v[52:55], v[102:105], v[16:19]
	v_mfma_f32_16x16x32_bf16 v[60:63], v[48:51], v[106:109], v[4:7]
	v_mfma_f32_16x16x32_bf16 v[4:7], v[44:47], v[102:105], v[20:23]
	v_mfma_f32_16x16x32_bf16 v[98:101], v[40:43], v[106:109], v[4:7]
	v_mfma_f32_16x16x32_bf16 v[4:7], v[52:55], v[110:113], v[24:27]
	v_mfma_f32_16x16x32_bf16 v[102:105], v[48:51], v[114:117], v[4:7]
	v_mfma_f32_16x16x32_bf16 v[4:7], v[44:47], v[110:113], v[28:31]
	v_mfma_f32_16x16x32_bf16 v[106:109], v[40:43], v[114:117], v[4:7]
	v_mfma_f32_16x16x32_bf16 v[4:7], v[52:55], v[118:121], v[32:35]
	v_mfma_f32_16x16x32_bf16 v[110:113], v[48:51], v[122:125], v[4:7]
	v_mfma_f32_16x16x32_bf16 v[4:7], v[44:47], v[118:121], v[36:39]
	v_mfma_f32_16x16x32_bf16 v[114:117], v[40:43], v[122:125], v[4:7]
	v_mfma_f32_16x16x32_bf16 v[4:7], v[52:55], v[130:133], v[8:11]
	v_mfma_f32_16x16x32_bf16 v[0:3], v[44:47], v[130:133], v[0:3]
	v_mfma_f32_16x16x32_bf16 v[118:121], v[48:51], v[134:137], v[4:7]
	v_mfma_f32_16x16x32_bf16 v[122:125], v[40:43], v[134:137], v[0:3]
	s_setprio 0
	s_barrier
	s_mov_b64 s[10:11], 0x300
	s_mov_b32 m0, s86
	s_nop 1
	v_lshl_add_u64 v[0:1], v[64:65], 0, s[10:11]
	global_load_lds_dwordx4 v[0:1], off
	v_lshl_add_u64 v[0:1], v[66:67], 0, s[10:11]
	s_add_u32 s10, s4, 0x200300
	s_mov_b32 m0, s87
	s_addc_u32 s11, s5, 0
	global_load_lds_dwordx4 v[0:1], off
	v_lshl_add_u64 v[0:1], s[10:11], 0, v[156:157]
	s_mov_b32 m0, s88
	s_nop 0
	global_load_lds_dwordx4 v[0:1], off
	v_lshl_add_u64 v[0:1], s[10:11], 0, v[158:159]
	s_mov_b32 m0, s89
	s_nop 0
	global_load_lds_dwordx4 v[0:1], off
	ds_read2_b32 v[0:1], v128 offset1:1
	s_mov_b32 m0, s67
	s_waitcnt lgkmcnt(0)
	global_load_lds_dwordx4 v0, s[18:19]
	s_mov_b32 m0, s68
	s_nop 0
	global_load_lds_dwordx4 v1, s[18:19]
	s_waitcnt vmcnt(8)
	s_waitcnt lgkmcnt(0)
	s_barrier
	s_barrier
	ds_read_b128 v[24:27], v68
	ds_read_b128 v[28:31], v68 offset:1024
	ds_read_b128 v[32:35], v68 offset:2048
	ds_read_b128 v[36:39], v68 offset:3072
	ds_read_b128 v[130:133], v69
	ds_read_b128 v[134:137], v69 offset:1024
	ds_read_b128 v[138:141], v69 offset:2048
	ds_read_b128 v[142:145], v69 offset:3072
	ds_read_b128 v[40:43], v184 offset:32768
	ds_read_b128 v[44:47], v184 offset:33792
	ds_read_b128 v[48:51], v184 offset:34816
	ds_read_b128 v[52:55], v184 offset:35840
	ds_read_b128 v[146:149], v184 offset:36864
	ds_read_b128 v[162:165], v184 offset:37888
	ds_read2_b32 v[0:1], v128 offset0:2 offset1:3
	ds_read_b128 v[166:169], v184 offset:38912
	ds_read_b128 v[170:173], v184 offset:39936
	s_mov_b32 m0, s69
	s_waitcnt lgkmcnt(0)
	global_load_lds_dwordx4 v0, s[18:19]
	s_mov_b32 m0, s70
	s_nop 0
	global_load_lds_dwordx4 v1, s[18:19]
	s_waitcnt vmcnt(8)
	s_waitcnt lgkmcnt(0)
	s_barrier
	s_setprio 1
	v_mfma_f32_16x16x32_bf16 v[0:3], v[24:27], v[40:43], v[70:73]
	v_mfma_f32_16x16x32_bf16 v[8:11], v[24:27], v[48:51], v[78:81]
	v_mfma_f32_16x16x32_bf16 v[16:19], v[24:27], v[146:149], v[86:89]
	v_mfma_f32_16x16x32_bf16 v[24:27], v[24:27], v[166:169], v[94:97]
	v_mfma_f32_16x16x32_bf16 v[0:3], v[28:31], v[44:47], v[0:3]
	v_mfma_f32_16x16x32_bf16 v[4:7], v[32:35], v[40:43], v[74:77]
	v_mfma_f32_16x16x32_bf16 v[8:11], v[28:31], v[52:55], v[8:11]
	v_mfma_f32_16x16x32_bf16 v[12:15], v[32:35], v[48:51], v[82:85]
	v_mfma_f32_16x16x32_bf16 v[16:19], v[28:31], v[162:165], v[16:19]
	v_mfma_f32_16x16x32_bf16 v[20:23], v[32:35], v[146:149], v[90:93]
	v_mfma_f32_16x16x32_bf16 v[24:27], v[28:31], v[170:173], v[24:27]
	v_mfma_f32_16x16x32_bf16 v[28:31], v[32:35], v[166:169], v[56:59]
	v_mfma_f32_16x16x32_bf16 v[4:7], v[36:39], v[44:47], v[4:7]
	v_mfma_f32_16x16x32_bf16 v[12:15], v[36:39], v[52:55], v[12:15]
	v_mfma_f32_16x16x32_bf16 v[20:23], v[36:39], v[162:165], v[20:23]
	v_mfma_f32_16x16x32_bf16 v[28:31], v[36:39], v[170:173], v[28:31]
	s_setprio 0
	s_setprio 1
	v_mfma_f32_16x16x32_bf16 v[32:35], v[130:133], v[40:43], v[60:63]
	v_mfma_f32_16x16x32_bf16 v[36:39], v[138:141], v[40:43], v[98:101]
	v_mfma_f32_16x16x32_bf16 v[32:35], v[134:137], v[44:47], v[32:35]
	v_mfma_f32_16x16x32_bf16 v[36:39], v[142:145], v[44:47], v[36:39]
	v_mfma_f32_16x16x32_bf16 v[40:43], v[130:133], v[48:51], v[102:105]
	v_mfma_f32_16x16x32_bf16 v[44:47], v[138:141], v[48:51], v[106:109]
	v_mfma_f32_16x16x32_bf16 v[40:43], v[134:137], v[52:55], v[40:43]
	v_mfma_f32_16x16x32_bf16 v[44:47], v[142:145], v[52:55], v[44:47]
	v_mfma_f32_16x16x32_bf16 v[48:51], v[130:133], v[146:149], v[110:113]
	v_mfma_f32_16x16x32_bf16 v[52:55], v[138:141], v[146:149], v[114:117]
	v_mfma_f32_16x16x32_bf16 v[56:59], v[130:133], v[166:169], v[118:121]
	v_mfma_f32_16x16x32_bf16 v[60:63], v[138:141], v[166:169], v[122:125]
	v_mfma_f32_16x16x32_bf16 v[48:51], v[134:137], v[162:165], v[48:51]
	v_mfma_f32_16x16x32_bf16 v[52:55], v[142:145], v[162:165], v[52:55]
	v_mfma_f32_16x16x32_bf16 v[56:59], v[134:137], v[170:173], v[56:59]
	v_mfma_f32_16x16x32_bf16 v[60:63], v[142:145], v[170:173], v[60:63]
	s_setprio 0
	s_barrier
	s_mov_b32 m0, s91
	v_lshl_add_u64 v[64:65], v[64:65], 0, s[54:55]
	s_add_u32 s10, s4, 0x200380
	global_load_lds_dwordx4 v[64:65], off
	v_lshl_add_u64 v[64:65], v[66:67], 0, s[54:55]
	s_mov_b32 m0, s90
	s_addc_u32 s11, s5, 0
	global_load_lds_dwordx4 v[64:65], off
	v_lshl_add_u64 v[64:65], s[10:11], 0, v[156:157]
	s_mov_b32 m0, s92
	s_nop 0
	global_load_lds_dwordx4 v[64:65], off
	v_lshl_add_u64 v[64:65], s[10:11], 0, v[158:159]
	s_mov_b32 m0, s93
	s_nop 0
	global_load_lds_dwordx4 v[64:65], off
	ds_read2_b32 v[64:65], v128 offset1:1
	s_mov_b32 m0, s71
	s_waitcnt lgkmcnt(0)
	global_load_lds_dwordx4 v64, s[52:53]
	s_mov_b32 m0, s72
	s_nop 0
	global_load_lds_dwordx4 v65, s[52:53]
	s_waitcnt vmcnt(8)
	s_waitcnt lgkmcnt(0)
	s_barrier
	s_barrier
	s_and_b64 vcc, exec, s[2:3]
	s_cbranch_vccnz .LBB0_2159
	s_and_saveexec_b64 s[10:11], s[0:1]
	s_cbranch_execz .LBB0_2158
	s_mov_b64 exec, 1
	s_lshl_b64 s[12:13], s[8:9], 2
	s_add_u32 s12, s94, s12
	v_readlane_b32 s14, v253, 2
	s_mov_b32 s36, s94
	s_addc_u32 s13, s14, s13
	s_mov_b32 s94, 0x400001
	s_branch .LBB0_2151

.LBB0_2162:
	s_cmp_eq_u32 s84, 6
	s_cselect_b64 s[10:11], -1, 0
	s_and_b64 s[12:13], s[6:7], s[10:11]
	s_andn2_b64 vcc, exec, s[12:13]
	s_cbranch_vccnz .LBB0_2174
	s_and_saveexec_b64 s[12:13], s[0:1]
	s_cbranch_execz .LBB0_2173
	s_mov_b64 exec, 1
	s_mov_b32 s85, 0x400001
	s_branch .LBB0_2166
